# m5o3_1
# speedup vs baseline: 1.0292x; 1.0292x over previous
_Z10gae_kernelPKfPKiS2_S0_S0_S0_PfS3_:
	s_load_dwordx8 s[4:11], s[0:1], 0x0
	s_load_dwordx4 s[12:15], s[0:1], 0x20
	v_and_b32_e32 v64, 63, v0
	v_lshrrev_b32_e32 v1, 6, v0
	s_andn2_b32 s16, s2, 63
	s_and_b32 s17, s2, 7
	s_lshl_b32 s17, s17, 3
	s_bfe_u32 s18, s2, 0x30003
	s_or_b32 s16, s16, s17
	s_or_b32 s2, s16, s18
	s_mov_b32 s3, 0
	s_lshl_b64 s[2:3], s[2:3], 11
	v_lshlrev_b32_e32 v2, 9, v1
	v_lshlrev_b32_e32 v3, 2, v64
	v_or3_b32 v2, s2, v2, v3
	v_mov_b32_e32 v3, s3
	v_lshlrev_b64 v[18:19], 2, v[2:3]
	s_waitcnt lgkmcnt(0)
	v_lshl_add_u64 v[54:55], s[14:15], 0, v[18:19]
	v_lshl_add_u64 v[52:53], s[6:7], 0, v[18:19]
	global_load_dwordx4 v[10:13], v[54:55], off nt
	global_load_dwordx4 v[14:17], v[52:53], off nt
	v_lshl_add_u64 v[56:57], s[8:9], 0, v[18:19]
	global_load_dwordx4 v[20:23], v[56:57], off nt
	v_lshl_add_u64 v[58:59], s[12:13], 0, v[18:19]
	global_load_dwordx4 v[24:27], v[58:59], off nt
	v_lshl_add_u64 v[60:61], s[4:5], 0, v[18:19]
	global_load_dwordx4 v[28:31], v[60:61], off nt
	v_lshl_add_u64 v[62:63], s[10:11], 0, v[18:19]
	global_load_dwordx4 v[2:5], v[62:63], off nt
	global_load_dwordx4 v[32:35], v[60:61], off offset:1024 nt
	global_load_dwordx4 v[36:39], v[52:53], off offset:1024 nt
	global_load_dwordx4 v[40:43], v[56:57], off offset:1024 nt
	global_load_dwordx4 v[6:9], v[62:63], off offset:1024 nt
	global_load_dwordx4 v[44:47], v[58:59], off offset:1024 nt
	global_load_dwordx4 v[48:51], v[54:55], off offset:1024 nt
	v_mov_b32_e32 v66, 0
	v_mov_b32_e32 v68, 1.0
	v_mov_b32_e32 v69, 0
	v_mov_b32_e32 v70, 1.0
	v_mov_b32_e32 v71, 0
	v_mov_b32_e32 v72, 1.0
	v_bfe_u32 v73, v0, 4, 2
	v_cmp_gt_u32_e64 s[4:5], 16, v64
	v_mov_b32_e32 v65, 0
	v_mov_b32_e32 v67, 1.0
	s_waitcnt vmcnt(11)
	v_mul_f32_e32 v12, 0x3f7d70a4, v12
	s_waitcnt vmcnt(10)
	v_cmp_eq_u32_e32 vcc, 0, v14
	v_mul_f32_e32 v13, 0x3f7d70a4, v13
	v_mul_f32_e32 v10, 0x3f7d70a4, v10
	v_cndmask_b32_e64 v14, 0, 1.0, vcc
	s_waitcnt vmcnt(9)
	v_cmp_eq_u32_e32 vcc, 0, v20
	v_mul_f32_e32 v11, 0x3f7d70a4, v11
	s_waitcnt vmcnt(8)
	v_mul_f32_e32 v26, v26, v12
	v_cndmask_b32_e64 v20, 0, 1.0, vcc
	v_cmp_eq_u32_e32 vcc, 0, v15
	v_mul_f32_e32 v27, v27, v13
	v_mul_f32_e32 v24, v24, v10
	v_cndmask_b32_e64 v15, 0, 1.0, vcc
	v_cmp_eq_u32_e32 vcc, 0, v21
	v_mul_f32_e32 v25, v25, v11
	v_mul_f32_e32 v12, 0x3f733333, v12
	v_cndmask_b32_e64 v21, 0, 1.0, vcc
	v_cmp_eq_u32_e32 vcc, 0, v16
	v_mul_f32_e32 v13, 0x3f733333, v13
	v_mul_f32_e32 v10, 0x3f733333, v10
	v_cndmask_b32_e64 v16, 0, 1.0, vcc
	v_cmp_eq_u32_e32 vcc, 0, v22
	s_waitcnt vmcnt(7)
	v_fma_f32 v16, v26, v16, v30
	v_mul_f32_e32 v11, 0x3f733333, v11
	v_cndmask_b32_e64 v22, 0, 1.0, vcc
	v_cmp_eq_u32_e32 vcc, 0, v17
	v_fma_f32 v14, v24, v14, v28
	v_fma_f32 v15, v25, v15, v29
	v_cndmask_b32_e64 v17, 0, 1.0, vcc
	v_cmp_eq_u32_e32 vcc, 0, v23
	v_fmac_f32_e32 v31, v27, v17
	v_mul_f32_e32 v22, v12, v22
	v_cndmask_b32_e64 v23, 0, 1.0, vcc
	v_mul_f32_e32 v23, v13, v23
	s_waitcnt vmcnt(6)
	v_sub_f32_e32 v12, v16, v4
	v_sub_f32_e32 v13, v31, v5
	v_mul_f32_e32 v20, v10, v20
	v_mul_f32_e32 v21, v11, v21
	v_sub_f32_e32 v10, v14, v2
	v_sub_f32_e32 v11, v15, v3
	v_mul_f32_e32 v14, v23, v22
	v_fma_f32 v15, v22, v13, v12
	v_mul_f32_e32 v14, v14, v21
	v_fma_f32 v15, v21, v15, v11
	v_mul_f32_e32 v14, v14, v20
	v_fma_f32 v24, v20, v15, v10
	v_mov_b32_e32 v16, 1.0
	v_mov_b32_dpp v68, v14 row_shl:1 row_mask:0xf bank_mask:0xf
	v_mov_b32_dpp v66, v24 row_shl:1 row_mask:0xf bank_mask:0xf
	v_mul_f32_e32 v15, v14, v68
	v_fmac_f32_e32 v24, v14, v66
	v_cmp_eq_u32_e32 vcc, 2, v73
	v_mov_b32_dpp v70, v15 row_shl:2 row_mask:0xf bank_mask:0xf
	v_mov_b32_dpp v69, v24 row_shl:2 row_mask:0xf bank_mask:0xf
	v_mul_f32_e32 v14, v15, v70
	v_fmac_f32_e32 v24, v15, v69
	v_mov_b32_e32 v15, 0
	v_mov_b32_dpp v72, v14 row_shl:4 row_mask:0xf bank_mask:0xf
	v_mov_b32_dpp v71, v24 row_shl:4 row_mask:0xf bank_mask:0xf
	v_fmac_f32_e32 v24, v14, v71
	v_mul_f32_e32 v14, v14, v72
	s_nop 0
	v_mov_b32_dpp v15, v24 row_shl:8 row_mask:0xf bank_mask:0xf
	v_mov_b32_dpp v16, v14 row_shl:8 row_mask:0xf bank_mask:0xf
	v_fmac_f32_e32 v24, v14, v15
	v_mul_f32_e32 v14, v14, v16
	v_readlane_b32 s9, v24, 32
	v_readlane_b32 s2, v14, 48
	v_readlane_b32 s8, v14, 32
	v_readlane_b32 s6, v14, 16
	v_mov_b32_e32 v15, s2
	v_mul_f32_e32 v16, s8, v15
	v_cndmask_b32_e32 v15, 1.0, v15, vcc
	v_cmp_eq_u32_e64 s[2:3], 1, v73
	v_readlane_b32 s10, v24, 48
	v_mul_f32_e32 v17, s6, v16
	v_cndmask_b32_e64 v15, v15, v16, s[2:3]
	v_readlane_b32 s7, v24, 16
	v_cndmask_b32_e64 v15, v15, v17, s[4:5]
	v_mov_b32_e32 v16, s9
	v_mov_b32_e32 v17, s10
	v_fmac_f32_e32 v16, s8, v17
	v_mov_b32_e32 v25, s7
	v_cndmask_b32_e32 v17, 0, v17, vcc
	v_fmac_f32_e32 v25, s6, v16
	v_cndmask_b32_e64 v16, v17, v16, s[2:3]
	v_cndmask_b32_e64 v16, v16, v25, s[4:5]
	s_waitcnt vmcnt(4)
	v_cmp_eq_u32_e64 s[6:7], 0, v36
	v_fmac_f32_e32 v24, v14, v16
	v_mul_f32_e32 v28, v14, v15
	s_waitcnt vmcnt(0)
	v_mul_f32_e32 v15, 0x3f7d70a4, v48
	v_cndmask_b32_e64 v14, 0, 1.0, s[6:7]
	v_cmp_eq_u32_e64 s[6:7], 0, v40
	v_mul_f32_e32 v17, v44, v15
	v_mul_f32_e32 v15, 0x3f733333, v15
	v_cndmask_b32_e64 v16, 0, 1.0, s[6:7]
	v_cmp_eq_u32_e64 s[6:7], 0, v37
	v_mul_f32_e32 v25, v15, v16
	v_mul_f32_e32 v16, 0x3f7d70a4, v49
	v_cndmask_b32_e64 v15, 0, 1.0, s[6:7]
	v_cmp_eq_u32_e64 s[6:7], 0, v41
	v_fma_f32 v14, v17, v14, v32
	v_mul_f32_e32 v26, v45, v16
	v_cndmask_b32_e64 v17, 0, 1.0, s[6:7]
	v_mul_f32_e32 v16, 0x3f733333, v16
	v_fma_f32 v15, v26, v15, v33
	v_mul_f32_e32 v26, v16, v17
	v_mul_f32_e32 v17, 0x3f7d70a4, v50
	v_cmp_eq_u32_e64 s[6:7], 0, v38
	v_mul_f32_e32 v29, v46, v17
	v_mul_f32_e32 v17, 0x3f733333, v17
	v_cndmask_b32_e64 v16, 0, 1.0, s[6:7]
	v_cmp_eq_u32_e64 s[6:7], 0, v42
	v_fma_f32 v16, v29, v16, v34
	v_mul_f32_e32 v29, 0x3f7d70a4, v51
	v_cndmask_b32_e64 v27, 0, 1.0, s[6:7]
	v_cmp_eq_u32_e64 s[6:7], 0, v39
	v_mul_f32_e32 v27, v17, v27
	v_mul_f32_e32 v31, v47, v29
	v_cndmask_b32_e64 v17, 0, 1.0, s[6:7]
	v_cmp_eq_u32_e64 s[6:7], 0, v43
	v_fmac_f32_e32 v35, v31, v17
	v_mul_f32_e32 v29, 0x3f733333, v29
	v_cndmask_b32_e64 v30, 0, 1.0, s[6:7]
	v_sub_f32_e32 v16, v16, v8
	v_sub_f32_e32 v17, v35, v9
	v_mul_f32_e32 v29, v29, v30
	v_sub_f32_e32 v15, v15, v7
	v_fma_f32 v30, v27, v17, v16
	v_mul_f32_e32 v31, v29, v27
	v_sub_f32_e32 v14, v14, v6
	v_fma_f32 v30, v26, v30, v15
	v_mul_f32_e32 v31, v31, v26
	v_fma_f32 v30, v25, v30, v14
	v_mul_f32_e32 v31, v31, v25
	v_mov_b32_e32 v32, 0
	v_mov_b32_e32 v33, 1.0
	s_nop 0
	v_mov_b32_dpp v32, v30 row_shl:1 row_mask:0xf bank_mask:0xf
	v_mov_b32_dpp v33, v31 row_shl:1 row_mask:0xf bank_mask:0xf
	v_fmac_f32_e32 v30, v31, v32
	v_mul_f32_e32 v31, v31, v33
	v_mov_b32_e32 v32, 0
	v_mov_b32_e32 v33, 1.0
	s_nop 0
	v_mov_b32_dpp v32, v30 row_shl:2 row_mask:0xf bank_mask:0xf
	v_mov_b32_dpp v33, v31 row_shl:2 row_mask:0xf bank_mask:0xf
	v_fmac_f32_e32 v30, v31, v32
	v_mul_f32_e32 v31, v31, v33
	v_mov_b32_e32 v32, 0
	v_mov_b32_e32 v33, 1.0
	s_nop 0
	v_mov_b32_dpp v32, v30 row_shl:4 row_mask:0xf bank_mask:0xf
	v_mov_b32_dpp v33, v31 row_shl:4 row_mask:0xf bank_mask:0xf
	v_fmac_f32_e32 v30, v31, v32
	v_mul_f32_e32 v31, v31, v33
	s_nop 0
	v_mov_b32_dpp v65, v30 row_shl:8 row_mask:0xf bank_mask:0xf
	v_mov_b32_dpp v67, v31 row_shl:8 row_mask:0xf bank_mask:0xf
	v_fmac_f32_e32 v30, v31, v65
	v_mul_f32_e32 v31, v31, v67
	v_readlane_b32 s9, v30, 32
	v_readlane_b32 s10, v31, 48
	v_readlane_b32 s8, v31, 32
	v_readlane_b32 s6, v31, 16
	v_mov_b32_e32 v32, s10
	v_mul_f32_e32 v33, s8, v32
	v_cndmask_b32_e32 v32, 1.0, v32, vcc
	v_readlane_b32 s11, v30, 48
	v_mul_f32_e32 v34, s6, v33
	v_cndmask_b32_e64 v32, v32, v33, s[2:3]
	v_readlane_b32 s7, v30, 16
	v_cndmask_b32_e64 v32, v32, v34, s[4:5]
	v_mov_b32_e32 v33, s9
	v_mov_b32_e32 v34, s11
	v_fmac_f32_e32 v33, s8, v34
	v_mov_b32_e32 v35, s7
	v_cndmask_b32_e32 v34, 0, v34, vcc
	v_fmac_f32_e32 v35, s6, v33
	v_cndmask_b32_e64 v33, v34, v33, s[2:3]
	v_cndmask_b32_e64 v33, v33, v35, s[4:5]
	v_fmac_f32_e32 v30, v31, v33
	v_mul_f32_e32 v31, v31, v32
	v_readlane_b32 s6, v28, 0
	v_readlane_b32 s7, v24, 0
	v_readlane_b32 s4, v31, 0
	v_readlane_b32 s5, v30, 0
	v_cmp_eq_u32_e32 vcc, 0, v64
	s_and_saveexec_b64 s[2:3], vcc
	s_cbranch_execz .LBB0_4
	v_mov_b32_e32 v32, s4
	v_mov_b32_e32 v33, s7
	v_mov_b32_e32 v34, s5
	v_mul_f32_e32 v32, s6, v32
	v_lshlrev_b32_e32 v1, 2, v1
	v_fmac_f32_e32 v33, s6, v34
	ds_write2_b32 v1, v32, v33 offset1:4
